# adds: attention queue atomic wait deferred; P0 x->bf16 loop double-buffered
# baseline (speedup 1.0000x reference)
; #define GAS __attribute__((address_space(1)))
; __device__ __forceinline__ unsigned pk2(float lo, float hi) { f32x2_t v = {lo, hi}; bf16x2_t b = __builtin_convertvector(v, bf16x2_t); return __builtin_bit_cast(unsigned, b); }
; #define LTID() const int tid_ = hw_tid(F.lds), lane_ = tid_ & 63, wave_ = __builtin_amdgcn_readfirstlane(tid_ >> 6); (void)lane_; (void)wave_
; __device__ __forceinline__ void p0_x_to_bf16(Frame& F, const float* x, bf16* XB) { LTID();
;     const int gw = F.vcu * NWAVES + wave_, NGW = F.G * NWAVES;
;     for (int m = gw; m < T; m += NGW) {
;         const GAS f32x4* xr = (const GAS f32x4*)(x + (size_t)m * D) + lane_; GAS v2u* o = (GAS v2u*)(XB + (size_t)m * D) + lane_;
; #pragma unroll
;         for (int j = 0; j < 4; ++j) { const f32x4 v = __builtin_nontemporal_load(xr + 64 * j); v2u w; w.x = pk2(v.x, v.y); w.y = pk2(v.z, v.w); o[64 * j] = w; } }
; }
.LBB0_65:
	s_or_b64 exec, exec, s[8:9]
	s_getreg_b32 s0, hwreg(HW_REG_HW_ID, 0, 6)
	s_lshl_b32 s0, s0, 2
	s_and_b32 s0, s0, 0xfc
	s_add_i32 s0, s0, 0
	s_add_i32 s0, s0, 0x23f00
	v_mov_b32_e32 v0, s0
	ds_read_b32 v0, v0
	s_waitcnt lgkmcnt(0)
	v_readfirstlane_b32 s0, v0
	v_mbcnt_lo_u32_b32 v1, -1, v1
	v_mbcnt_hi_u32_b32 v0, -1, v1
	v_lshl_add_u32 v0, s0, 6, v0
	s_nop 0
	v_readfirstlane_b32 s0, v0
	s_ashr_i32 s1, s0, 6
	v_readlane_b32 s0, v253, 11
	s_add_i32 s0, s1, s0
	s_cmpk_gt_i32 s0, 0x7fff
	s_cbranch_scc1 .LBB0_68
	s_load_dwordx2 s[2:3], s[4:5], 0x0
	v_readlane_b32 s8, v253, 11
	s_ashr_i32 s4, s1, 31
	s_ashr_i32 s5, s8, 31
	s_add_u32 s8, s1, s8
	s_addc_u32 s9, s4, s5
	s_lshl_b64 s[4:5], s[8:9], 12
	s_waitcnt vmcnt(6)
	v_and_b32_e32 v4, 63, v0
	s_waitcnt lgkmcnt(0)
	s_add_u32 s2, s2, s4
	v_lshlrev_b32_e32 v2, 4, v4
	v_mov_b32_e32 v3, 0
	s_addc_u32 s3, s3, s5
	v_lshl_add_u64 v[0:1], s[2:3], 0, v[2:3]
	s_mov_b64 s[2:3], 0x800
	s_ashr_i32 s45, s44, 31
	v_lshl_add_u64 v[0:1], v[0:1], 0, s[2:3]
	s_lshl_b64 s[4:5], s[44:45], 12
	s_lshl_b64 s[2:3], s[8:9], 11
	s_add_u32 s2, s6, s2
	v_lshlrev_b32_e32 v2, 3, v4
	s_addc_u32 s3, s7, s3
	v_lshl_add_u64 v[2:3], s[2:3], 0, v[2:3]
	s_mov_b64 s[2:3], 0x34000400
	v_lshl_add_u64 v[2:3], v[2:3], 0, s[2:3]
	s_lshl_b64 s[6:7], s[44:45], 11
	s_waitcnt vmcnt(0)
	global_load_dwordx4 v[4:7], v[0:1], off offset:-2048 nt
	global_load_dwordx4 v[8:11], v[0:1], off offset:-1024 nt
	global_load_dwordx4 v[12:15], v[0:1], off nt
	global_load_dwordx4 v[16:19], v[0:1], off offset:1024 nt
	v_lshl_add_u64 v[0:1], v[0:1], 0, s[4:5]
.Lx2b_loop:
	s_add_i32 s0, s0, s44
	s_cmp_lt_i32 s0, 0x8000
	s_cbranch_scc0 .Lx2b_lastA
	global_load_dwordx4 v[20:23], v[0:1], off offset:-2048 nt
	global_load_dwordx4 v[24:27], v[0:1], off offset:-1024 nt
	global_load_dwordx4 v[28:31], v[0:1], off nt
	global_load_dwordx4 v[32:35], v[0:1], off offset:1024 nt
	v_lshl_add_u64 v[0:1], v[0:1], 0, s[4:5]
	s_waitcnt vmcnt(4)
	v_cvt_pk_bf16_f32 v4, v4, v5
	v_cvt_pk_bf16_f32 v5, v6, v7
	global_store_dwordx2 v[2:3], v[4:5], off offset:-1024
	v_cvt_pk_bf16_f32 v8, v8, v9
	v_cvt_pk_bf16_f32 v9, v10, v11
	global_store_dwordx2 v[2:3], v[8:9], off offset:-512
	v_cvt_pk_bf16_f32 v12, v12, v13
	v_cvt_pk_bf16_f32 v13, v14, v15
	global_store_dwordx2 v[2:3], v[12:13], off
	v_cvt_pk_bf16_f32 v16, v16, v17
	v_cvt_pk_bf16_f32 v17, v18, v19
	global_store_dwordx2 v[2:3], v[16:17], off offset:512
	v_lshl_add_u64 v[2:3], v[2:3], 0, s[6:7]
	s_add_i32 s0, s0, s44
	s_cmp_lt_i32 s0, 0x8000
	s_cbranch_scc0 .Lx2b_lastB
	global_load_dwordx4 v[4:7], v[0:1], off offset:-2048 nt
	global_load_dwordx4 v[8:11], v[0:1], off offset:-1024 nt
	global_load_dwordx4 v[12:15], v[0:1], off nt
	global_load_dwordx4 v[16:19], v[0:1], off offset:1024 nt
	v_lshl_add_u64 v[0:1], v[0:1], 0, s[4:5]
	s_waitcnt vmcnt(4)
	v_cvt_pk_bf16_f32 v20, v20, v21
	v_cvt_pk_bf16_f32 v21, v22, v23
	global_store_dwordx2 v[2:3], v[20:21], off offset:-1024
	v_cvt_pk_bf16_f32 v24, v24, v25
	v_cvt_pk_bf16_f32 v25, v26, v27
	global_store_dwordx2 v[2:3], v[24:25], off offset:-512
	v_cvt_pk_bf16_f32 v28, v28, v29
	v_cvt_pk_bf16_f32 v29, v30, v31
	global_store_dwordx2 v[2:3], v[28:29], off
	v_cvt_pk_bf16_f32 v32, v32, v33
	v_cvt_pk_bf16_f32 v33, v34, v35
	global_store_dwordx2 v[2:3], v[32:33], off offset:512
	v_lshl_add_u64 v[2:3], v[2:3], 0, s[6:7]
	s_branch .Lx2b_loop
.Lx2b_lastA:
	s_waitcnt vmcnt(0)
	v_cvt_pk_bf16_f32 v4, v4, v5
	v_cvt_pk_bf16_f32 v5, v6, v7
	global_store_dwordx2 v[2:3], v[4:5], off offset:-1024
	v_cvt_pk_bf16_f32 v8, v8, v9
	v_cvt_pk_bf16_f32 v9, v10, v11
	global_store_dwordx2 v[2:3], v[8:9], off offset:-512
	v_cvt_pk_bf16_f32 v12, v12, v13
	v_cvt_pk_bf16_f32 v13, v14, v15
	global_store_dwordx2 v[2:3], v[12:13], off
	v_cvt_pk_bf16_f32 v16, v16, v17
	v_cvt_pk_bf16_f32 v17, v18, v19
	global_store_dwordx2 v[2:3], v[16:17], off offset:512
	v_lshl_add_u64 v[2:3], v[2:3], 0, s[6:7]
	s_branch .LBB0_68
.Lx2b_lastB:
	s_waitcnt vmcnt(0)
	v_cvt_pk_bf16_f32 v20, v20, v21
	v_cvt_pk_bf16_f32 v21, v22, v23
	global_store_dwordx2 v[2:3], v[20:21], off offset:-1024
	v_cvt_pk_bf16_f32 v24, v24, v25
	v_cvt_pk_bf16_f32 v25, v26, v27
	global_store_dwordx2 v[2:3], v[24:25], off offset:-512
	v_cvt_pk_bf16_f32 v28, v28, v29
	v_cvt_pk_bf16_f32 v29, v30, v31
	global_store_dwordx2 v[2:3], v[28:29], off
	v_cvt_pk_bf16_f32 v32, v32, v33
	v_cvt_pk_bf16_f32 v33, v34, v35
	global_store_dwordx2 v[2:3], v[32:33], off offset:512
	v_lshl_add_u64 v[2:3], v[2:3], 0, s[6:7]
